# gate|up GEMM prologue: row-index waits recounted to allow the already-issued B-operand LDS-DMA pieces in flight (A pieces issue without draining them)
# baseline (speedup 1.0000x reference)
; #define PG8_STAGEB(bufoff, gbase) glds2(voffB, (gbase), voffB, (gbase) + qstep, ldsb + (bufoff))
; #define PG8_STAGEA(bufoff, rowb, v, h, kb) do { if constexpr (GATHER) glds2((v)[h][0], Ab + (kb), (v)[h][1], Ab + (kb), ldsb + (bufoff)); \
;         else glds2(voffA, Ab + (rowb) + (h) * hstep + (kb), voffA, Ab + (rowb) + (h) * hstep + qstep + (kb), ldsb + (bufoff)); } while (0)
; #define PG8_VOFF(dst, U) do { if constexpr (GATHER) { _Pragma("unroll") for (int h = 0; h < 2; ++h) _Pragma("unroll") for (int i = 0; i < 2; ++i) { \
;         const int row = g.rowidx[(U).pm * BM + h * HALF + i * 64 + R0]; dst[h][i] = (unsigned)row * (unsigned)RB + (unsigned)C0 * 2u; } } } while (0)
;     __device__ bool next(int i, Unit& u) const {
;         const long L = (long)i * G + c; if (L >= nwg) return false;
;         int wgid = (int)L; { const int q = nwg / NXCD, r = nwg % NXCD, xcd = wgid % NXCD, off = wgid / NXCD; wgid = (xcd < r ? xcd * (q + 1) : r * (q + 1) + (xcd - r) * q) + off; }
;         const int nig = wgm * nN, gid = wgid / nig, fm = gid * wgm, gsz = (nM - fm) < wgm ? (nM - fm) : wgm;
;         u.pm = fm + ((wgid % nig) % gsz); u.pn = (wgid % nig) / gsz; if (u.pn >= gap_at) u.pn += gap; u.e = tile_e ? tile_e[u.pm] : 0; return true;
;     }
; template <class Epi, bool GATHER, int MODE, bool SPLIT = false>
; __device__ __forceinline__ void gemm_phase(PG8_LAS unsigned char* lds, const Gemm g, const Order& S, const Epi& E) {
;     ...
;     Unit cur, nxt; int ui = 0;
;     if (!S.next(0, cur)) return;
;     f32x4 acc[2][2][4][2];
; #pragma unroll
;     for (int a = 0; a < 2; ++a)
; #pragma unroll
;         for (int b = 0; b < 2; ++b)
; #pragma unroll
;             for (int m = 0; m < 4; ++m)
; #pragma unroll
;                 for (int n = 0; n < 2; ++n) acc[a][b][m][n] = (f32x4){0.f, 0.f, 0.f, 0.f};
;     bf16x8 At[4][2], B0[2][2], B1[2][2];
;     unsigned cv[2][2] = {{0u, 0u}, {0u, 0u}}, nv[2][2] = {{0u, 0u}, {0u, 0u}};
;     PG8_VOFF(cv, cur);
;     const char* const Ab = (const char*)g.A;
;     size_t cAr = (size_t)cur.pm * tstep;
;     const char* cB = (const char*)g.Bt + (size_t)cur.e * g.bstride + (size_t)cur.pn * tstep;
;     PG8_STAGEB(PG8_SB(0, 0), cB); PG8_STAGEB(PG8_SB(0, 1), cB + hstep); PG8_STAGEA(PG8_SA(0, 0), cAr, cv, 0, 0); PG8_STAGEA(PG8_SA(0, 1), cAr, cv, 1, 0);
.LBB0_790:
	s_cmp_lt_i32 s78, 9
	s_cselect_b64 s[0:1], -1, 0
	s_cmp_gt_i32 s79, 8
	s_cselect_b64 s[2:3], -1, 0
	s_and_b64 s[0:1], s[0:1], s[2:3]
	s_andn2_b64 vcc, exec, s[0:1]
	s_cbranch_vccnz .LBB0_863
	v_mov_b32_e32 v1, 0xc00000
	global_load_dword v1, v1, s[76:77] offset:2048
	s_waitcnt vmcnt(20)
	v_mov_b32_e32 v2, v0
	s_waitcnt vmcnt(0)
	v_readfirstlane_b32 s38, v1
	s_lshl_b32 s2, s38, 4
	s_cmp_ge_i32 s92, s2
	v_readfirstlane_b32 s3, v2
	s_cbranch_scc1 .LBB0_809
	s_add_u32 s39, s76, 0xc00000
	s_addc_u32 s40, s77, 0
	s_add_u32 s6, s76, 0x5b000000
	s_addc_u32 s7, s77, 0
	s_add_u32 s41, s76, 0x28000000
	s_addc_u32 s42, s77, 0
	s_add_u32 s8, s76, 0xb00000
	s_addc_u32 s9, s77, 0
	s_ashr_i32 s4, s3, 6
	s_lshl_b32 s0, s4, 10
	s_ashr_i32 s45, s92, 31
	s_add_i32 s43, s0, 0
	s_lshr_b32 s0, s45, 29
	s_add_i32 s0, s92, s0
	s_lshl_b32 s44, s38, 1
	s_ashr_i32 s1, s0, 3
	s_and_b32 s0, s0, -8
	s_ashr_i32 s5, s3, 8
	s_sub_i32 s0, s92, s0
	s_or_b32 s46, s44, 1
	s_cmp_lt_i32 s0, 0
	s_cselect_b32 s10, s46, s44
	s_mul_i32 s0, s10, s0
	s_add_i32 s0, s0, s1
	s_ashr_i32 s1, s0, 31
	s_lshr_b32 s1, s1, 26
	s_add_i32 s1, s0, s1
	v_bfe_i32 v4, v2, 27, 1
	s_ashr_i32 s10, s1, 6
	v_lshlrev_b32_e32 v1, 4, v2
	v_lshrrev_b32_e32 v4, 22, v4
	s_lshl_b32 s10, s10, 2
	v_add_u32_e32 v4, v1, v4
	s_sub_i32 s11, s38, s10
	v_and_b32_e32 v4, 0xfffffc00, v4
	s_min_i32 s11, s11, 4
	v_sub_u32_e32 v1, v1, v4
	s_abs_i32 s12, s11
	v_lshrrev_b32_e32 v4, 4, v1
	v_cvt_f32_u32_e32 v5, s12
	v_bitop3_b32 v12, v4, v1, 32 bitop3:0x6c
	v_ashrrev_i32_e32 v4, 31, v12
	v_lshrrev_b32_e32 v4, 26, v4
	v_add_u32_e32 v13, v12, v4
	v_rcp_iflag_f32_e32 v4, v5
	s_sub_i32 s14, 0, s12
	s_andn2_b32 s1, s1, 63
	s_sub_i32 s1, s0, s1
	v_mul_f32_e32 v4, 0x4f7ffffe, v4
	v_cvt_u32_f32_e32 v4, v4
	s_abs_i32 s13, s1
	s_xor_b32 s0, s1, s11
	s_ashr_i32 s0, s0, 31
	v_readfirstlane_b32 s15, v4
	s_mul_i32 s14, s14, s15
	s_mul_hi_u32 s14, s15, s14
	s_add_i32 s15, s15, s14
	s_mul_hi_u32 s14, s13, s15
	s_mul_i32 s15, s14, s12
	s_sub_i32 s13, s13, s15
	s_add_i32 s15, s14, 1
	s_sub_i32 s16, s13, s12
	s_cmp_ge_u32 s13, s12
	s_cselect_b32 s14, s15, s14
	s_cselect_b32 s13, s16, s13
	s_add_i32 s15, s14, 1
	v_ashrrev_i32_e32 v3, 31, v2
	s_cmp_ge_u32 s13, s12
	v_lshrrev_b32_e32 v3, 26, v3
	s_cselect_b32 s12, s15, s14
	v_add_u32_e32 v3, v2, v3
	s_xor_b32 s12, s12, s0
	v_ashrrev_i32_e32 v3, 6, v3
	s_sub_i32 s0, s12, s0
	v_lshlrev_b32_e32 v1, 3, v3
	s_mul_i32 s11, s0, s11
	v_and_b32_e32 v1, -16, v1
	v_ashrrev_i32_e32 v14, 6, v13
	s_sub_i32 s1, s1, s11
	v_add_u32_e32 v1, v14, v1
	s_add_i32 s10, s10, s1
	s_ashr_i32 s11, s10, 31
	v_lshl_add_u32 v4, s10, 8, v1
	s_lshl_b64 s[12:13], s[10:11], 2
	v_ashrrev_i32_e32 v5, 31, v4
	s_add_u32 s12, s39, s12
	v_lshl_add_u64 v[6:7], v[4:5], 2, s[8:9]
	v_add_u32_e32 v8, 64, v4
	v_add_u32_e32 v10, 0x80, v4
	v_add_u32_e32 v4, 0xc0, v4
	s_addc_u32 s13, s40, s13
	v_mov_b32_e32 v166, 0
	v_ashrrev_i32_e32 v9, 31, v8
	v_ashrrev_i32_e32 v11, 31, v10
	v_ashrrev_i32_e32 v5, 31, v4
	v_lshl_add_u64 v[8:9], v[8:9], 2, s[8:9]
	v_lshl_add_u64 v[10:11], v[10:11], 2, s[8:9]
	v_lshl_add_u64 v[4:5], v[4:5], 2, s[8:9]
	global_load_dword v164, v166, s[12:13]
	global_load_dword v15, v[6:7], off
	global_load_dword v16, v[8:9], off
	global_load_dword v17, v[10:11], off
	global_load_dword v18, v[4:5], off
	s_mov_b32 s1, 0x1fffe0
	v_and_b32_e32 v6, 3, v14
	v_and_or_b32 v6, v1, s1, v6
	v_and_b32_e32 v5, 0xc0, v13
	v_mov_b32_e32 v4, 1
	v_sub_u32_e32 v5, v12, v5
	v_lshlrev_b32_e32 v3, 5, v3
	v_ashrrev_i16_sdwa v4, v4, sext(v5) dst_sel:DWORD dst_unused:UNUSED_PAD src0_sel:DWORD src1_sel:BYTE_0
	v_lshlrev_b32_e32 v5, 1, v1
	v_lshrrev_b32_e32 v7, 2, v1
	v_and_b32_e32 v3, 32, v3
	v_bfe_i32 v4, v4, 0, 16
	v_and_b32_e32 v5, 24, v5
	v_and_b32_e32 v7, 4, v7
	v_or3_b32 v5, v6, v7, v5
	v_add_lshl_u32 v167, v3, v4, 1
	v_lshl_add_u32 v168, v5, 11, v167
	s_mov_b32 s47, 0
	s_movk_i32 s48, 0x2000
	s_waitcnt vmcnt(4)
	v_readfirstlane_b32 s12, v164
	s_ashr_i32 s13, s12, 31
	s_lshl_b64 s[12:13], s[12:13], 23
	s_add_u32 s11, s41, s12
	s_addc_u32 s14, s42, s13
	s_ashr_i32 s1, s0, 31
	s_lshl_b64 s[12:13], s[0:1], 19
	s_add_u32 s34, s11, s12
	s_addc_u32 s35, s14, s13
	s_add_u32 s12, s34, 0x20000
	s_addc_u32 s13, s35, 0
	s_add_i32 s49, s43, 0x10000
	s_add_i32 s50, s43, 0x12000
	s_mov_b32 s1, m0
	s_mov_b32 m0, s49
	s_nop 0
	global_load_lds_dwordx4 v168, s[34:35]
	s_mov_b32 m0, s50
	s_nop 0
	global_load_lds_dwordx4 v168, s[12:13]
	s_mov_b32 m0, s1
	s_add_u32 s12, s34, 0x40000
	s_addc_u32 s13, s35, 0
	s_add_u32 s14, s34, 0x60000
	s_addc_u32 s15, s35, 0
	s_add_i32 s51, s43, 0x14000
	s_add_i32 s52, s43, 0x16000
	s_mov_b32 s1, m0
	s_mov_b32 m0, s51
	s_nop 0
	global_load_lds_dwordx4 v168, s[12:13]
	s_mov_b32 m0, s52
	s_nop 0
	global_load_lds_dwordx4 v168, s[14:15]
	s_mov_b32 m0, s1
	s_waitcnt vmcnt(7)
	v_lshl_add_u32 v191, v15, 11, v167
	s_waitcnt vmcnt(6)
	v_lshl_add_u32 v192, v16, 11, v167
	s_add_i32 s53, s43, 0x2000
	s_mov_b32 s1, m0
	s_mov_b32 m0, s43
	s_nop 0
	global_load_lds_dwordx4 v191, s[6:7]
	s_mov_b32 m0, s53
	s_nop 0
	global_load_lds_dwordx4 v192, s[6:7]
	s_mov_b32 m0, s1
	s_waitcnt vmcnt(7)
	v_lshl_add_u32 v189, v17, 11, v167
	s_waitcnt vmcnt(6)
	v_lshl_add_u32 v190, v18, 11, v167
	s_add_i32 s54, s43, 0x4000
	s_add_i32 s55, s43, 0x6000
	s_mov_b32 s1, m0
	s_mov_b32 m0, s54
	s_nop 0
	global_load_lds_dwordx4 v189, s[6:7]
	s_mov_b32 m0, s55
	s_nop 0
	global_load_lds_dwordx4 v190, s[6:7]
	s_mov_b32 m0, s1
	s_cmp_eq_u32 s5, 1
	s_cselect_b64 s[12:13], -1, 0
	s_cmp_lg_u32 s5, 1
	s_cbranch_scc1 .LBB0_794
	s_barrier
